# speedup vs baseline: 1.0541x; 1.0040x over previous
.Llight_path:
	s_waitcnt vmcnt(0)
	v_mul_u32_u24_e32 v236, 36, v228
	v_add_u32_e32 v236, v236, v230
	v_add_u32_e32 v237, s7, v229
	v_mul_u32_u24_e32 v238, 0x104, v228
	v_add_u32_e32 v238, v238, v237
	v_add_u32_e32 v238, 0xb840, v238
	ds_read_b128 v[2:5], v237 offset:36928
	ds_read_b128 v[6:9], v237 offset:36944
	ds_read_b128 v[10:13], v237 offset:36960
	ds_read_b128 v[14:17], v237 offset:36976
	ds_read_b128 v[18:21], v237 offset:37056
	ds_read_b128 v[22:25], v237 offset:37072
	ds_read_b128 v[26:29], v237 offset:37088
	ds_read_b128 v[30:33], v237 offset:37104
	ds_read_b128 v[162:165], v236 offset:16384
	ds_read_b128 v[166:169], v236 offset:16416
	ds_read_b128 v[170:173], v236 offset:16448
	ds_read_b128 v[174:177], v236 offset:16480
	s_waitcnt lgkmcnt(0)
	v_mfma_f32_32x32x16_bf16 v[2:17], v[94:97], v[162:165], v[2:17]
	v_mfma_f32_32x32x16_bf16 v[2:17], v[90:93], v[166:169], v[2:17]
	v_mfma_f32_32x32x16_bf16 v[2:17], v[86:89], v[170:173], v[2:17]
	v_mfma_f32_32x32x16_bf16 v[2:17], v[82:85], v[174:177], v[2:17]
	v_mfma_f32_32x32x16_bf16 v[18:33], v[46:49], v[162:165], v[18:33]
	ds_read_b128 v[130:133], v237 offset:36928
	ds_read_b128 v[134:137], v237 offset:36944
	ds_read_b128 v[138:141], v237 offset:36960
	v_mfma_f32_32x32x16_bf16 v[18:33], v[42:45], v[166:169], v[18:33]
	ds_read_b128 v[142:145], v237 offset:36976
	ds_read_b128 v[146:149], v237 offset:37056
	ds_read_b128 v[150:153], v237 offset:37072
	v_mfma_f32_32x32x16_bf16 v[18:33], v[38:41], v[170:173], v[18:33]
	ds_read_b128 v[154:157], v237 offset:37088
	ds_read_b128 v[158:161], v237 offset:37104
	ds_read_b128 v[178:181], v236 offset:20992
	v_mfma_f32_32x32x16_bf16 v[18:33], v[34:37], v[174:177], v[18:33]
	ds_read_b128 v[182:185], v236 offset:21024
	ds_read_b128 v[186:189], v236 offset:21056
	ds_read_b128 v[190:193], v236 offset:21088
	s_waitcnt lgkmcnt(0)
	v_mfma_f32_32x32x16_bf16 v[130:145], v[94:97], v[178:181], v[130:145]
	v_mfma_f32_32x32x16_bf16 v[130:145], v[90:93], v[182:185], v[130:145]
	v_mfma_f32_32x32x16_bf16 v[130:145], v[86:89], v[186:189], v[130:145]
	v_mfma_f32_32x32x16_bf16 v[130:145], v[82:85], v[190:193], v[130:145]
	s_nop 7
	ds_write_b128 v238, v[2:5] offset:0
	ds_write_b128 v238, v[6:9] offset:16
	ds_write_b128 v238, v[10:13] offset:32
	ds_write_b128 v238, v[14:17] offset:48
	ds_write_b128 v238, v[18:21] offset:128
	ds_write_b128 v238, v[22:25] offset:144
	ds_write_b128 v238, v[26:29] offset:160
	ds_write_b128 v238, v[30:33] offset:176
	v_mfma_f32_32x32x16_bf16 v[146:161], v[46:49], v[178:181], v[146:161]
	ds_read_b128 v[2:5], v237 offset:36928
	ds_read_b128 v[6:9], v237 offset:36944
	ds_read_b128 v[10:13], v237 offset:36960
	v_mfma_f32_32x32x16_bf16 v[146:161], v[42:45], v[182:185], v[146:161]
	ds_read_b128 v[14:17], v237 offset:36976
	ds_read_b128 v[18:21], v237 offset:37056
	ds_read_b128 v[22:25], v237 offset:37072
	v_mfma_f32_32x32x16_bf16 v[146:161], v[38:41], v[186:189], v[146:161]
	ds_read_b128 v[26:29], v237 offset:37088
	ds_read_b128 v[30:33], v237 offset:37104
	ds_read_b128 v[162:165], v236 offset:25600
	v_mfma_f32_32x32x16_bf16 v[146:161], v[34:37], v[190:193], v[146:161]
	ds_read_b128 v[166:169], v236 offset:25632
	ds_read_b128 v[170:173], v236 offset:25664
	ds_read_b128 v[174:177], v236 offset:25696
	s_waitcnt lgkmcnt(0)
	v_mfma_f32_32x32x16_bf16 v[2:17], v[94:97], v[162:165], v[2:17]
	v_mfma_f32_32x32x16_bf16 v[2:17], v[90:93], v[166:169], v[2:17]
	v_mfma_f32_32x32x16_bf16 v[2:17], v[86:89], v[170:173], v[2:17]
	v_mfma_f32_32x32x16_bf16 v[2:17], v[82:85], v[174:177], v[2:17]
	s_nop 7
	v_add_u32_e32 v239, 0x8200, v238
	ds_write_b128 v239, v[130:133] offset:0
	ds_write_b128 v239, v[134:137] offset:16
	ds_write_b128 v239, v[138:141] offset:32
	ds_write_b128 v239, v[142:145] offset:48
	ds_write_b128 v239, v[146:149] offset:128
	ds_write_b128 v239, v[150:153] offset:144
	ds_write_b128 v239, v[154:157] offset:160
	ds_write_b128 v239, v[158:161] offset:176
	v_mfma_f32_32x32x16_bf16 v[18:33], v[46:49], v[162:165], v[18:33]
	ds_read_b128 v[130:133], v237 offset:36928
	ds_read_b128 v[134:137], v237 offset:36944
	ds_read_b128 v[138:141], v237 offset:36960
	v_mfma_f32_32x32x16_bf16 v[18:33], v[42:45], v[166:169], v[18:33]
	ds_read_b128 v[142:145], v237 offset:36976
	ds_read_b128 v[146:149], v237 offset:37056
	ds_read_b128 v[150:153], v237 offset:37072
	v_mfma_f32_32x32x16_bf16 v[18:33], v[38:41], v[170:173], v[18:33]
	ds_read_b128 v[154:157], v237 offset:37088
	ds_read_b128 v[158:161], v237 offset:37104
	ds_read_b128 v[178:181], v236 offset:30208
	v_mfma_f32_32x32x16_bf16 v[18:33], v[34:37], v[174:177], v[18:33]
	ds_read_b128 v[182:185], v236 offset:30240
	ds_read_b128 v[186:189], v236 offset:30272
	ds_read_b128 v[190:193], v236 offset:30304
	s_waitcnt lgkmcnt(0)
	v_mfma_f32_32x32x16_bf16 v[130:145], v[94:97], v[178:181], v[130:145]
	v_mfma_f32_32x32x16_bf16 v[130:145], v[90:93], v[182:185], v[130:145]
	v_mfma_f32_32x32x16_bf16 v[130:145], v[86:89], v[186:189], v[130:145]
	v_mfma_f32_32x32x16_bf16 v[130:145], v[82:85], v[190:193], v[130:145]
	s_nop 7
	v_add_u32_e32 v239, 0x10400, v238
	ds_write_b128 v239, v[2:5] offset:0
	ds_write_b128 v239, v[6:9] offset:16
	ds_write_b128 v239, v[10:13] offset:32
	ds_write_b128 v239, v[14:17] offset:48
	ds_write_b128 v239, v[18:21] offset:128
	ds_write_b128 v239, v[22:25] offset:144
	ds_write_b128 v239, v[26:29] offset:160
	ds_write_b128 v239, v[30:33] offset:176
	v_mfma_f32_32x32x16_bf16 v[146:161], v[46:49], v[178:181], v[146:161]
	v_mfma_f32_32x32x16_bf16 v[146:161], v[42:45], v[182:185], v[146:161]
	v_mfma_f32_32x32x16_bf16 v[146:161], v[38:41], v[186:189], v[146:161]
	v_mfma_f32_32x32x16_bf16 v[146:161], v[34:37], v[190:193], v[146:161]
	s_nop 7
	s_nop 7
	v_cmp_gt_u32_e32 vcc, 16, v228
	s_and_saveexec_b64 s[20:21], vcc
	v_add_u32_e32 v239, 0x18600, v238
	ds_write_b128 v239, v[130:133] offset:0
	ds_write_b128 v239, v[134:137] offset:16
	ds_write_b128 v239, v[138:141] offset:32
	ds_write_b128 v239, v[142:145] offset:48
	ds_write_b128 v239, v[146:149] offset:128
	ds_write_b128 v239, v[150:153] offset:144
	ds_write_b128 v239, v[154:157] offset:160
	ds_write_b128 v239, v[158:161] offset:176
	s_or_b64 exec, exec, s[20:21]
	s_waitcnt vmcnt(0) lgkmcnt(0)
	s_nop 7
	s_nop 7
	v_add_u32_e32 v231, s7, v229
	v_add_u32_e32 v231, 0xb840, v231
	v_add_u32_e32 v211, s6, v210
	s_mov_b32 s12, 0x4038aa3b
	v_mov_b32_e32 v235, 0xc038aa3b
	s_nop 0
	s_load_dwordx8 s[4:11], s[0:1], 0x10
	s_waitcnt lgkmcnt(0)
	v_add_u32_e32 v232, 0x24e80, v228
	ds_read_b32 v244, v232
	ds_read_b32 v245, v232 offset:128
	v_mov_b32_e32 v194, 0
	v_mov_b32_e32 v195, 0
	v_mov_b32_e32 v196, 0
	v_mov_b32_e32 v197, 0
	v_mov_b32_e32 v198, 0
	v_mov_b32_e32 v199, 0
	v_mov_b32_e32 v200, 0
	v_mov_b32_e32 v201, 0
	v_mov_b32_e32 v202, 0
	v_mov_b32_e32 v203, 0
	v_mov_b32_e32 v204, 0
	v_mov_b32_e32 v205, 0
	v_mov_b32_e32 v206, 0
	v_mov_b32_e32 v207, 0
	v_mov_b32_e32 v208, 0
	v_mov_b32_e32 v209, 0
	v_add_u32_e32 v232, 0x100, v232
	s_waitcnt lgkmcnt(0)
	v_add_u32_e32 v233, v231, v244
	v_add_u32_e32 v234, v231, v245
	ds_read_b128 v[2:5], v233 offset:0
	ds_read_b128 v[6:9], v233 offset:16
	ds_read_b128 v[10:13], v233 offset:32
	ds_read_b128 v[14:17], v233 offset:48
	ds_read_b128 v[18:21], v233 offset:128
	ds_read_b128 v[22:25], v233 offset:144
	ds_read_b128 v[26:29], v233 offset:160
	ds_read_b128 v[30:33], v233 offset:176
	ds_read_b128 v[34:37], v234 offset:0
	ds_read_b128 v[38:41], v234 offset:16
	ds_read_b128 v[42:45], v234 offset:32
	ds_read_b128 v[46:49], v234 offset:48
	s_movk_i32 s16, 18
	s_waitcnt lgkmcnt(0)
	ds_read_b128 v[82:85], v234 offset:128
	ds_read_b128 v[86:89], v234 offset:144
	ds_read_b128 v[90:93], v234 offset:160
	ds_read_b128 v[94:97], v234 offset:176
	ds_read_b32 v244, v232 offset:0
	v_exp_f32_e32 v212, v4
	v_exp_f32_e32 v213, v8
	v_exp_f32_e32 v214, v12
	v_exp_f32_e32 v215, v16
	v_exp_f32_e32 v216, v2
	v_exp_f32_e32 v217, v6
	v_exp_f32_e32 v218, v10
	v_exp_f32_e32 v219, v14
	v_add_f32_e32 v236, 1.0, v212
	v_add_f32_e32 v237, 1.0, v213
	v_add_f32_e32 v238, 1.0, v214
	v_add_f32_e32 v239, 1.0, v215
	v_fma_f32 v240, v212, s12, v235
	v_fma_f32 v241, v213, s12, v235
	v_fma_f32 v242, v214, s12, v235
	v_fma_f32 v243, v215, s12, v235
	v_fmac_f32_e32 v236, v216, v236
	v_fmac_f32_e32 v237, v217, v237
	v_fmac_f32_e32 v238, v218, v238
	v_fmac_f32_e32 v239, v219, v239
	v_rcp_f32_e32 v216, v236
	v_rcp_f32_e32 v217, v237
	v_rcp_f32_e32 v218, v238
	v_rcp_f32_e32 v219, v239
	v_exp_f32_e32 v224, v5
	v_exp_f32_e32 v225, v9
	v_exp_f32_e32 v226, v13
	v_exp_f32_e32 v227, v17
	v_mul_f32_e32 v194, v240, v216
	v_mul_f32_e32 v195, v241, v217
	v_mul_f32_e32 v196, v242, v218
	v_mul_f32_e32 v197, v243, v219
	v_exp_f32_e32 v212, v194
	v_exp_f32_e32 v213, v195
	v_exp_f32_e32 v214, v196
	v_exp_f32_e32 v215, v197
	v_add_f32_e32 v224, 1.0, v224
	v_add_f32_e32 v225, 1.0, v225
	v_add_f32_e32 v226, 1.0, v226
	v_add_f32_e32 v227, 1.0, v227
	v_fmac_f32_e32 v224, v224, v212
	v_fmac_f32_e32 v225, v225, v213
	v_fmac_f32_e32 v226, v226, v214
	v_fmac_f32_e32 v227, v227, v215
	v_rcp_f32_e32 v224, v224
	v_rcp_f32_e32 v225, v225
	v_rcp_f32_e32 v226, v226
	v_rcp_f32_e32 v227, v227
	v_fma_f32 v224, -v212, v224, v224
	v_fma_f32 v225, -v213, v225, v225
	v_fma_f32 v226, -v214, v226, v226
	v_fma_f32 v227, -v215, v227, v227
	v_cvt_pk_bf16_f32 v224, v224, v225
	v_cvt_pk_bf16_f32 v225, v226, v227
	ds_write_b64 v211, v[224:225] offset:0
	s_waitcnt lgkmcnt(1)
	v_add_u32_e32 v233, v231, v244
	ds_read_b128 v[2:5], v233 offset:0
	ds_read_b128 v[6:9], v233 offset:16
	ds_read_b128 v[10:13], v233 offset:32
	ds_read_b128 v[14:17], v233 offset:48
	v_exp_f32_e32 v212, v20
	v_exp_f32_e32 v213, v24
	v_exp_f32_e32 v214, v28
	v_exp_f32_e32 v215, v32
	v_exp_f32_e32 v216, v18
	v_exp_f32_e32 v217, v22
	v_exp_f32_e32 v218, v26
	v_exp_f32_e32 v219, v30
	v_add_f32_e32 v236, 1.0, v212
	v_add_f32_e32 v237, 1.0, v213
	v_add_f32_e32 v238, 1.0, v214
	v_add_f32_e32 v239, 1.0, v215
	v_fma_f32 v240, v212, s12, v235
	v_fma_f32 v241, v213, s12, v235
	v_fma_f32 v242, v214, s12, v235
	v_fma_f32 v243, v215, s12, v235
	v_fmac_f32_e32 v236, v216, v236
	v_fmac_f32_e32 v237, v217, v237
	v_fmac_f32_e32 v238, v218, v238
	v_fmac_f32_e32 v239, v219, v239
	v_rcp_f32_e32 v216, v236
	v_rcp_f32_e32 v217, v237
	v_rcp_f32_e32 v218, v238
	v_rcp_f32_e32 v219, v239
	v_exp_f32_e32 v224, v21
	v_exp_f32_e32 v225, v25
	v_exp_f32_e32 v226, v29
	v_exp_f32_e32 v227, v33
	v_mul_f32_e32 v198, v240, v216
	v_mul_f32_e32 v199, v241, v217
	v_mul_f32_e32 v200, v242, v218
	v_mul_f32_e32 v201, v243, v219
	v_exp_f32_e32 v212, v198
	v_exp_f32_e32 v213, v199
	v_exp_f32_e32 v214, v200
	v_exp_f32_e32 v215, v201
	v_add_f32_e32 v224, 1.0, v224
	v_add_f32_e32 v225, 1.0, v225
	v_add_f32_e32 v226, 1.0, v226
	v_add_f32_e32 v227, 1.0, v227
	v_fmac_f32_e32 v224, v224, v212
	v_fmac_f32_e32 v225, v225, v213
	v_fmac_f32_e32 v226, v226, v214
	v_fmac_f32_e32 v227, v227, v215
	v_rcp_f32_e32 v224, v224
	v_rcp_f32_e32 v225, v225
	v_rcp_f32_e32 v226, v226
	v_rcp_f32_e32 v227, v227
	v_fma_f32 v224, -v212, v224, v224
	v_fma_f32 v225, -v213, v225, v225
	v_fma_f32 v226, -v214, v226, v226
	v_fma_f32 v227, -v215, v227, v227
	v_cvt_pk_bf16_f32 v224, v224, v225
	v_cvt_pk_bf16_f32 v225, v226, v227
	ds_write_b64 v211, v[224:225] offset:8
	s_waitcnt lgkmcnt(0)
	s_barrier
	ds_read_b128 v[130:133], v210 offset:0
	ds_read_b128 v[134:137], v210 offset:1024
	ds_read_b128 v[18:21], v233 offset:128
	ds_read_b128 v[22:25], v233 offset:144
	ds_read_b128 v[26:29], v233 offset:160
	ds_read_b128 v[30:33], v233 offset:176
	ds_read_b32 v245, v232 offset:128
	v_exp_f32_e32 v212, v36
	v_exp_f32_e32 v213, v40
	v_exp_f32_e32 v214, v44
	v_exp_f32_e32 v215, v48
	ds_read_b128 v[138:141], v210 offset:2048
	ds_read_b128 v[142:145], v210 offset:3072
	v_exp_f32_e32 v216, v34
	v_exp_f32_e32 v217, v38
	v_exp_f32_e32 v218, v42
	v_exp_f32_e32 v219, v46
	v_add_f32_e32 v236, 1.0, v212
	v_add_f32_e32 v237, 1.0, v213
	v_add_f32_e32 v238, 1.0, v214
	v_add_f32_e32 v239, 1.0, v215
	v_fma_f32 v240, v212, s12, v235
	v_fma_f32 v241, v213, s12, v235
	v_fma_f32 v242, v214, s12, v235
	v_fma_f32 v243, v215, s12, v235
	ds_read_b128 v[146:149], v210 offset:4096
	ds_read_b128 v[150:153], v210 offset:5120
	v_fmac_f32_e32 v236, v216, v236
	v_fmac_f32_e32 v237, v217, v237
	v_fmac_f32_e32 v238, v218, v238
	v_fmac_f32_e32 v239, v219, v239
	ds_read_b128 v[154:157], v210 offset:6144
	ds_read_b128 v[158:161], v210 offset:7168
	v_rcp_f32_e32 v216, v236
	v_rcp_f32_e32 v217, v237
	v_rcp_f32_e32 v218, v238
	v_rcp_f32_e32 v219, v239
	v_exp_f32_e32 v224, v37
	v_exp_f32_e32 v225, v41
	v_exp_f32_e32 v226, v45
	v_exp_f32_e32 v227, v49
	v_mul_f32_e32 v202, v240, v216
	v_mul_f32_e32 v203, v241, v217
	v_mul_f32_e32 v204, v242, v218
	v_mul_f32_e32 v205, v243, v219
	v_exp_f32_e32 v212, v202
	v_exp_f32_e32 v213, v203
	v_exp_f32_e32 v214, v204
	v_exp_f32_e32 v215, v205
	v_add_f32_e32 v224, 1.0, v224
	v_add_f32_e32 v225, 1.0, v225
	v_add_f32_e32 v226, 1.0, v226
	v_add_f32_e32 v227, 1.0, v227
	v_fmac_f32_e32 v224, v224, v212
	v_fmac_f32_e32 v225, v225, v213
	v_fmac_f32_e32 v226, v226, v214
	v_fmac_f32_e32 v227, v227, v215
	v_rcp_f32_e32 v224, v224
	v_rcp_f32_e32 v225, v225
	v_rcp_f32_e32 v226, v226
	v_rcp_f32_e32 v227, v227
	v_fma_f32 v224, -v212, v224, v224
	v_fma_f32 v225, -v213, v225, v225
	v_fma_f32 v226, -v214, v226, v226
	v_fma_f32 v227, -v215, v227, v227
	v_cvt_pk_bf16_f32 v224, v224, v225
	v_cvt_pk_bf16_f32 v225, v226, v227
	ds_write_b64 v211, v[224:225] offset:8192
	s_waitcnt lgkmcnt(1)
	v_mfma_f32_32x32x16_bf16 v[2:17], v[126:129], v[130:133], v[2:17]
	v_add_u32_e32 v234, v231, v245
	ds_read_b128 v[34:37], v234 offset:0
	ds_read_b128 v[38:41], v234 offset:16
	ds_read_b128 v[42:45], v234 offset:32
	ds_read_b128 v[46:49], v234 offset:48
	v_add_u32_e32 v232, 0x100, v232
	v_exp_f32_e32 v212, v84
	v_exp_f32_e32 v213, v88
	v_exp_f32_e32 v214, v92
	v_exp_f32_e32 v215, v96
	v_mfma_f32_32x32x16_bf16 v[2:17], v[122:125], v[134:137], v[2:17]
	v_exp_f32_e32 v216, v82
	v_exp_f32_e32 v217, v86
	v_exp_f32_e32 v218, v90
	v_exp_f32_e32 v219, v94
	v_add_f32_e32 v236, 1.0, v212
	v_add_f32_e32 v237, 1.0, v213
	v_add_f32_e32 v238, 1.0, v214
	v_add_f32_e32 v239, 1.0, v215
	v_fma_f32 v240, v212, s12, v235
	v_fma_f32 v241, v213, s12, v235
	v_fma_f32 v242, v214, s12, v235
	v_fma_f32 v243, v215, s12, v235
	v_mfma_f32_32x32x16_bf16 v[2:17], v[118:121], v[138:141], v[2:17]
	v_fmac_f32_e32 v236, v216, v236
	v_fmac_f32_e32 v237, v217, v237
	v_fmac_f32_e32 v238, v218, v238
	v_fmac_f32_e32 v239, v219, v239
	v_mfma_f32_32x32x16_bf16 v[2:17], v[114:117], v[142:145], v[2:17]
	v_rcp_f32_e32 v216, v236
	v_rcp_f32_e32 v217, v237
	v_rcp_f32_e32 v218, v238
	v_rcp_f32_e32 v219, v239
	v_mfma_f32_32x32x16_bf16 v[2:17], v[110:113], v[146:149], v[2:17]
	v_exp_f32_e32 v224, v85
	v_exp_f32_e32 v225, v89
	v_exp_f32_e32 v226, v93
	v_exp_f32_e32 v227, v97
	v_mul_f32_e32 v206, v240, v216
	v_mul_f32_e32 v207, v241, v217
	v_mul_f32_e32 v208, v242, v218
	v_mul_f32_e32 v209, v243, v219
	v_mfma_f32_32x32x16_bf16 v[2:17], v[106:109], v[150:153], v[2:17]
	v_mfma_f32_32x32x16_bf16 v[2:17], v[102:105], v[154:157], v[2:17]
	v_exp_f32_e32 v212, v206
	v_exp_f32_e32 v213, v207
	v_exp_f32_e32 v214, v208
	v_exp_f32_e32 v215, v209
	v_add_f32_e32 v224, 1.0, v224
	v_add_f32_e32 v225, 1.0, v225
	v_add_f32_e32 v226, 1.0, v226
	v_add_f32_e32 v227, 1.0, v227
	v_fmac_f32_e32 v224, v224, v212
	v_fmac_f32_e32 v225, v225, v213
	v_fmac_f32_e32 v226, v226, v214
	v_fmac_f32_e32 v227, v227, v215
	v_mfma_f32_32x32x16_bf16 v[2:17], v[98:101], v[158:161], v[2:17]
	v_rcp_f32_e32 v224, v224
	v_rcp_f32_e32 v225, v225
	v_rcp_f32_e32 v226, v226
	v_rcp_f32_e32 v227, v227
	v_fma_f32 v224, -v212, v224, v224
	v_fma_f32 v225, -v213, v225, v225
	v_fma_f32 v226, -v214, v226, v226
	v_fma_f32 v227, -v215, v227, v227
	v_cvt_pk_bf16_f32 v224, v224, v225
	v_cvt_pk_bf16_f32 v225, v226, v227
	ds_write_b64 v211, v[224:225] offset:8200
	s_waitcnt lgkmcnt(0)
	s_barrier
	.p2align 6
